# P0 transposes: next item's tile loads no longer wait for the previous item's stores (vmcnt(0) at item head removed)
# baseline (speedup 1.0000x reference)
.LBB0_64:
	s_lshr_b32 s24, s4, 7
	v_cvt_f32_u32_e32 v0, s24
	s_sub_i32 s25, 0, s24
	s_xor_b64 s[34:35], s[2:3], -1
	s_ashr_i32 s2, s58, 2
	v_rcp_iflag_f32_e32 v0, v0
	s_abs_i32 s3, s2
	v_mul_f32_e32 v0, 0x4f7ffffe, v0
	v_cvt_u32_f32_e32 v0, v0
	s_nop 0
	v_readfirstlane_b32 s36, v0
	s_mul_i32 s25, s25, s36
	s_mul_hi_u32 s25, s36, s25
	s_add_i32 s36, s36, s25
	s_mul_hi_u32 s25, s3, s36
	s_mul_i32 s36, s25, s24
	s_sub_i32 s3, s3, s36
	s_add_i32 s37, s25, 1
	s_sub_i32 s36, s3, s24
	s_cmp_ge_u32 s3, s24
	s_cselect_b32 s25, s37, s25
	s_cselect_b32 s3, s36, s3
	s_add_i32 s36, s25, 1
	s_cmp_ge_u32 s3, s24
	s_cselect_b32 s3, s36, s25
	s_ashr_i32 s59, s58, 31
	s_xor_b32 s3, s3, s59
	s_sub_i32 s3, s3, s59
	s_mul_i32 s24, s3, s24
	s_lshl_b32 s3, s3, 6
	v_or_b32_e32 v0, s3, v136
	s_ashr_i32 s3, s3, 31
	s_sub_i32 s2, s2, s24
	s_mul_i32 s3, s3, s4
	v_mad_u64_u32 v[0:1], s[24:25], v0, s4, 0
	s_lshl_b32 s2, s2, 7
	v_add_u32_e32 v1, s3, v1
	s_waitcnt lgkmcnt(0)
	v_lshl_add_u64 v[0:1], v[0:1], 2, s[0:1]
	s_ashr_i32 s3, s2, 31
	v_lshl_add_u64 v[0:1], s[2:3], 2, v[0:1]
	v_lshl_add_u64 v[0:1], v[0:1], 0, v[142:143]
	s_lshl_b64 s[0:1], s[4:5], 5
	v_lshl_add_u64 v[2:3], v[0:1], 0, s[0:1]
	v_lshl_add_u64 v[4:5], v[2:3], 0, s[0:1]
	global_load_dwordx4 v[120:123], v[2:3], off nt
	global_load_dwordx4 v[116:119], v[4:5], off nt
	v_lshl_add_u64 v[2:3], v[4:5], 0, s[0:1]
	v_lshl_add_u64 v[4:5], v[2:3], 0, s[0:1]
	global_load_dwordx4 v[108:111], v[2:3], off nt
	global_load_dwordx4 v[100:103], v[4:5], off nt
	v_lshl_add_u64 v[2:3], v[4:5], 0, s[0:1]
	v_lshl_add_u64 v[4:5], v[2:3], 0, s[0:1]
	v_lshl_add_u64 v[6:7], v[4:5], 0, s[0:1]
	v_mad_u64_u32 v[8:9], s[2:3], s4, v164, v[6:7]
	v_subrev_u32_e32 v9, s4, v9
	v_lshl_add_u64 v[10:11], v[8:9], 0, s[0:1]
	v_lshl_add_u64 v[12:13], v[10:11], 0, s[0:1]
	v_lshl_add_u64 v[14:15], v[12:13], 0, s[0:1]
	v_lshl_add_u64 v[16:17], v[14:15], 0, s[0:1]
	v_lshl_add_u64 v[18:19], v[16:17], 0, s[0:1]
	v_lshl_add_u64 v[20:21], v[18:19], 0, s[0:1]
	v_mad_u64_u32 v[22:23], s[2:3], s4, v164, v[20:21]
	v_subrev_u32_e32 v23, s4, v23
	v_lshl_add_u64 v[24:25], v[22:23], 0, s[0:1]
	v_lshl_add_u64 v[26:27], v[24:25], 0, s[0:1]
	v_lshl_add_u64 v[28:29], v[26:27], 0, s[0:1]
	v_lshl_add_u64 v[30:31], v[28:29], 0, s[0:1]
	v_lshl_add_u64 v[32:33], v[30:31], 0, s[0:1]
	v_lshl_add_u64 v[34:35], v[32:33], 0, s[0:1]
	v_mad_u64_u32 v[128:129], s[2:3], s4, v164, v[34:35]
	global_load_dwordx4 v[112:115], v[2:3], off nt
	global_load_dwordx4 v[104:107], v[4:5], off nt
	global_load_dwordx4 v[96:99], v[6:7], off nt
	global_load_dwordx4 v[88:91], v[8:9], off offset:128 nt
	global_load_dwordx4 v[84:87], v[10:11], off offset:128 nt
	global_load_dwordx4 v[80:83], v[12:13], off offset:128 nt
	global_load_dwordx4 v[76:79], v[14:15], off offset:128 nt
	global_load_dwordx4 v[72:75], v[16:17], off offset:128 nt
	global_load_dwordx4 v[68:71], v[18:19], off offset:128 nt
	global_load_dwordx4 v[64:67], v[20:21], off offset:128 nt
	global_load_dwordx4 v[56:59], v[22:23], off offset:256 nt
	global_load_dwordx4 v[52:55], v[24:25], off offset:256 nt
	global_load_dwordx4 v[48:51], v[26:27], off offset:256 nt
	global_load_dwordx4 v[44:47], v[28:29], off offset:256 nt
	global_load_dwordx4 v[40:43], v[30:31], off offset:256 nt
	global_load_dwordx4 v[36:39], v[32:33], off offset:256 nt
	s_nop 0
	global_load_dwordx4 v[32:35], v[34:35], off offset:256 nt
	s_nop 0
	global_load_dwordx4 v[124:127], v[0:1], off nt
	global_load_dwordx4 v[92:95], v[0:1], off offset:128 nt
	global_load_dwordx4 v[60:63], v[0:1], off offset:256 nt
	global_load_dwordx4 v[28:31], v[0:1], off offset:384 nt
	v_subrev_u32_e32 v129, s4, v129
	v_lshl_add_u64 v[0:1], v[128:129], 0, s[0:1]
	v_lshl_add_u64 v[2:3], v[0:1], 0, s[0:1]
	global_load_dwordx4 v[20:23], v[0:1], off offset:384 nt
	v_lshl_add_u64 v[0:1], v[2:3], 0, s[0:1]
	global_load_dwordx4 v[16:19], v[2:3], off offset:384 nt
	v_lshl_add_u64 v[2:3], v[0:1], 0, s[0:1]
	global_load_dwordx4 v[12:15], v[0:1], off offset:384 nt
	v_lshl_add_u64 v[0:1], v[2:3], 0, s[0:1]
	global_load_dwordx4 v[8:11], v[2:3], off offset:384 nt
	v_lshl_add_u64 v[2:3], v[0:1], 0, s[0:1]
	global_load_dwordx4 v[24:27], v[128:129], off offset:384 nt
	global_load_dwordx4 v[4:7], v[0:1], off offset:384 nt
	s_nop 0
	global_load_dwordx4 v[0:3], v[2:3], off offset:384 nt
	s_lshr_b32 s4, s4, 5
	v_cvt_f32_u32_e32 v128, s4
	s_sub_i32 s3, 0, s4
	s_abs_i32 s2, s58
	s_mov_b64 s[0:1], -1
	v_rcp_iflag_f32_e32 v128, v128
	s_nop 0
	v_mul_f32_e32 v128, 0x4f7ffffe, v128
	v_cvt_u32_f32_e32 v128, v128
	s_nop 0
	v_readfirstlane_b32 s56, v128
	s_mul_i32 s3, s3, s56
	s_mul_hi_u32 s3, s56, s3
	s_add_i32 s56, s56, s3
	s_mul_hi_u32 s3, s2, s56
	s_mul_i32 s24, s3, s4
	s_sub_i32 s60, s2, s24
	s_add_i32 s2, s3, 1
	s_sub_i32 s61, s60, s4
	s_cmp_ge_u32 s60, s4
	s_cselect_b32 s2, s2, s3
	s_cselect_b32 s3, s61, s60
	s_add_i32 s24, s2, 1
	s_cmp_ge_u32 s3, s4
	s_cselect_b32 s2, s24, s2
	s_xor_b32 s2, s2, s59
	s_sub_i32 s38, s2, s59
	s_lshl_b32 s36, s38, 6
	s_cmp_lg_u64 s[22:23], 0
	s_cselect_b64 s[24:25], -1, 0
	s_and_b64 vcc, exec, s[34:35]
	s_cbranch_vccz .LBB0_125
	s_cmp_lt_i32 s57, 1
	s_cbranch_scc1 .LBB0_110
	s_cmp_lt_i32 s57, 2
	s_cbranch_scc1 .LBB0_95
	s_cmp_lg_u32 s57, 2
	s_cbranch_scc0 .LBB0_81
	v_cndmask_b32_e64 v128, 0, 1, s[24:25]
	v_cmp_ne_u32_e64 s[2:3], 1, v128
	s_andn2_b64 vcc, exec, s[24:25]
	s_cbranch_vccnz .LBB0_854
	v_or_b32_e32 v128, s36, v136
	s_ashr_i32 s37, s36, 31
	v_ashrrev_i32_e32 v129, 31, v128
	v_lshl_add_u64 v[130:131], s[36:37], 0, v[136:137]
	v_lshl_add_u64 v[128:129], v[128:129], 2, s[22:23]
	v_lshl_add_u64 v[130:131], v[130:131], 2, s[22:23]
	global_load_dword v128, v[128:129], off
	s_nop 0
	global_load_dword v132, v[130:131], off offset:32
	s_waitcnt vmcnt(1)
	v_pk_mul_f32 v[134:135], v[126:127], v[128:129] op_sel_hi:[1,0]
	v_pk_mul_f32 v[168:169], v[124:125], v[128:129] op_sel_hi:[1,0]
	s_waitcnt vmcnt(0)
	v_pk_mul_f32 v[130:131], v[122:123], v[132:133] op_sel_hi:[1,0]
	v_pk_mul_f32 v[128:129], v[120:121], v[132:133] op_sel_hi:[1,0]
	ds_write2_b32 v145, v168, v169 offset1:1
	ds_write2_b32 v145, v134, v135 offset0:2 offset1:3
	s_cbranch_execnz .LBB0_71
